# v14_gemm
# speedup vs baseline: 1.0074x; 1.0074x over previous
_Z9k_gemm_byPKfS0_S0_PfS1_Pd:
	s_load_dwordx2 s[4:5], s[0:1], 0x10
	v_lshlrev_b32_e32 v1, 2, v0
	v_mov_b32_e32 v3, 0
	s_cmpk_gt_i32 s2, 0xff
	s_waitcnt lgkmcnt(0)
	global_load_dword v144, v1, s[4:5]
	global_load_dword v145, v1, s[4:5] offset:1024
	s_cbranch_scc1 .LBB0_4
	s_lshl_b32 s3, s2, 1
	v_bfe_u32 v7, v0, 5, 1
	s_movk_i32 s8, 0xffe0
	s_lshl_b32 s9, s2, 5
	v_mov_b32_e32 v2, s3
	s_load_dwordx2 s[6:7], s[0:1], 0x0
	s_load_dwordx2 s[4:5], s[0:1], 0x18
	v_and_b32_e32 v5, 31, v0
	v_lshrrev_b32_e32 v6, 6, v0
	s_and_b32 s9, s9, 0x1e0
	v_bfi_b32 v8, s8, v2, v0
	v_lshlrev_b32_e32 v2, 9, v7
	v_or_b32_e32 v4, s9, v5
	v_lshl_or_b32 v9, v6, 16, v2
	v_add_u32_e32 v10, v9, v8
	v_or_b32_e32 v2, v4, v9
	v_ashrrev_i32_e32 v11, 31, v10
	v_lshlrev_b32_e32 v32, 2, v2
	v_or_b32_e32 v2, 0x400, v9
	s_waitcnt lgkmcnt(0)
	v_lshl_add_u64 v[18:19], v[10:11], 2, s[6:7]
	v_add_u32_e32 v10, v2, v8
	v_or_b32_e32 v2, v4, v2
	v_ashrrev_i32_e32 v11, 31, v10
	v_lshl_add_u64 v[22:23], v[2:3], 2, s[6:7]
	v_or_b32_e32 v2, 0x800, v9
	v_lshl_add_u64 v[20:21], v[10:11], 2, s[6:7]
	v_add_u32_e32 v10, v2, v8
	v_or_b32_e32 v2, v4, v2
	v_ashrrev_i32_e32 v11, 31, v10
	v_lshl_add_u64 v[26:27], v[2:3], 2, s[6:7]
	v_or_b32_e32 v2, 0xc00, v9
	v_lshl_add_u64 v[24:25], v[10:11], 2, s[6:7]
	v_add_u32_e32 v10, v2, v8
	v_or_b32_e32 v2, v4, v2
	v_ashrrev_i32_e32 v11, 31, v10
	v_lshl_add_u64 v[30:31], v[2:3], 2, s[6:7]
	v_or_b32_e32 v2, 0x1000, v9
	v_lshl_add_u64 v[28:29], v[10:11], 2, s[6:7]
	global_load_dword v15, v[18:19], off
	global_load_dword v16, v32, s[6:7]
	global_load_dword v17, v[20:21], off
	global_load_dword v14, v[22:23], off
	global_load_dword v13, v[24:25], off
	global_load_dword v11, v[26:27], off
	global_load_dword v12, v[28:29], off
	global_load_dword v10, v[30:31], off
	v_add_u32_e32 v18, v2, v8
	v_or_b32_e32 v2, v4, v2
	v_ashrrev_i32_e32 v19, 31, v18
	v_lshl_add_u64 v[28:29], v[2:3], 2, s[6:7]
	v_or_b32_e32 v2, 0x1400, v9
	v_lshl_add_u64 v[26:27], v[18:19], 2, s[6:7]
	v_add_u32_e32 v18, v2, v8
	v_or_b32_e32 v2, v4, v2
	v_ashrrev_i32_e32 v19, 31, v18
	v_lshl_add_u64 v[32:33], v[2:3], 2, s[6:7]
	v_or_b32_e32 v2, 0x1800, v9
	v_lshl_add_u64 v[30:31], v[18:19], 2, s[6:7]
	v_add_u32_e32 v18, v2, v8
	v_or_b32_e32 v2, v4, v2
	v_ashrrev_i32_e32 v19, 31, v18
	v_lshl_add_u64 v[36:37], v[2:3], 2, s[6:7]
	v_or_b32_e32 v2, 0x1c00, v9
	v_lshl_add_u64 v[34:35], v[18:19], 2, s[6:7]
	v_add_u32_e32 v18, v2, v8
	v_or_b32_e32 v2, v4, v2
	v_ashrrev_i32_e32 v19, 31, v18
	v_lshl_add_u64 v[40:41], v[2:3], 2, s[6:7]
	v_or_b32_e32 v2, 0x2000, v9
	v_lshl_add_u64 v[38:39], v[18:19], 2, s[6:7]
	global_load_dword v25, v[26:27], off
	global_load_dword v23, v[28:29], off
	global_load_dword v24, v[30:31], off
	global_load_dword v22, v[32:33], off
	global_load_dword v21, v[34:35], off
	global_load_dword v19, v[36:37], off
	global_load_dword v20, v[38:39], off
	global_load_dword v18, v[40:41], off
	v_add_u32_e32 v26, v2, v8
	v_or_b32_e32 v2, v4, v2
	v_ashrrev_i32_e32 v27, 31, v26
	v_lshl_add_u64 v[36:37], v[2:3], 2, s[6:7]
	v_or_b32_e32 v2, 0x2400, v9
	v_lshl_add_u64 v[34:35], v[26:27], 2, s[6:7]
	v_add_u32_e32 v26, v2, v8
	v_or_b32_e32 v2, v4, v2
	v_ashrrev_i32_e32 v27, 31, v26
	v_lshl_add_u64 v[40:41], v[2:3], 2, s[6:7]
	v_or_b32_e32 v2, 0x2800, v9
	v_lshl_add_u64 v[38:39], v[26:27], 2, s[6:7]
	v_add_u32_e32 v26, v2, v8
	v_or_b32_e32 v2, v4, v2
	v_ashrrev_i32_e32 v27, 31, v26
	v_lshl_add_u64 v[44:45], v[2:3], 2, s[6:7]
	v_or_b32_e32 v2, 0x2c00, v9
	v_lshl_add_u64 v[42:43], v[26:27], 2, s[6:7]
	v_add_u32_e32 v26, v2, v8
	v_or_b32_e32 v2, v4, v2
	v_ashrrev_i32_e32 v27, 31, v26
	v_lshl_add_u64 v[48:49], v[2:3], 2, s[6:7]
	v_or_b32_e32 v2, 0x3000, v9
	v_lshl_add_u64 v[46:47], v[26:27], 2, s[6:7]
	global_load_dword v33, v[34:35], off
	global_load_dword v31, v[36:37], off
	global_load_dword v32, v[38:39], off
	global_load_dword v30, v[40:41], off
	global_load_dword v29, v[42:43], off
	global_load_dword v27, v[44:45], off
	global_load_dword v28, v[46:47], off
	global_load_dword v26, v[48:49], off
	v_add_u32_e32 v34, v2, v8
	v_or_b32_e32 v2, v4, v2
	v_ashrrev_i32_e32 v35, 31, v34
	v_lshl_add_u64 v[44:45], v[2:3], 2, s[6:7]
	v_or_b32_e32 v2, 0x3400, v9
	v_lshl_add_u64 v[42:43], v[34:35], 2, s[6:7]
	v_add_u32_e32 v34, v2, v8
	v_or_b32_e32 v2, v4, v2
	v_ashrrev_i32_e32 v35, 31, v34
	v_lshl_add_u64 v[48:49], v[2:3], 2, s[6:7]
	v_or_b32_e32 v2, 0x3800, v9
	v_lshl_add_u64 v[46:47], v[34:35], 2, s[6:7]
	v_add_u32_e32 v34, v2, v8
	v_or_b32_e32 v2, v4, v2
	v_ashrrev_i32_e32 v35, 31, v34
	v_lshl_add_u64 v[52:53], v[2:3], 2, s[6:7]
	v_or_b32_e32 v2, 0x3c00, v9
	v_lshl_add_u64 v[50:51], v[34:35], 2, s[6:7]
	v_add_u32_e32 v34, v2, v8
	v_or_b32_e32 v2, v4, v2
	v_ashrrev_i32_e32 v35, 31, v34
	v_lshl_add_u64 v[56:57], v[2:3], 2, s[6:7]
	v_or_b32_e32 v2, 0x4000, v9
	v_lshl_add_u64 v[54:55], v[34:35], 2, s[6:7]
	global_load_dword v41, v[42:43], off
	global_load_dword v39, v[44:45], off
	global_load_dword v40, v[46:47], off
	global_load_dword v38, v[48:49], off
	global_load_dword v37, v[50:51], off
	global_load_dword v35, v[52:53], off
	global_load_dword v36, v[54:55], off
	global_load_dword v34, v[56:57], off
	v_add_u32_e32 v42, v2, v8
	v_or_b32_e32 v2, v4, v2
	v_ashrrev_i32_e32 v43, 31, v42
	v_lshl_add_u64 v[52:53], v[2:3], 2, s[6:7]
	v_or_b32_e32 v2, 0x4400, v9
	v_lshl_add_u64 v[50:51], v[42:43], 2, s[6:7]
	v_add_u32_e32 v42, v2, v8
	v_or_b32_e32 v2, v4, v2
	v_ashrrev_i32_e32 v43, 31, v42
	v_lshl_add_u64 v[56:57], v[2:3], 2, s[6:7]
	v_or_b32_e32 v2, 0x4800, v9
	v_lshl_add_u64 v[54:55], v[42:43], 2, s[6:7]
	v_add_u32_e32 v42, v2, v8
	v_or_b32_e32 v2, v4, v2
	v_ashrrev_i32_e32 v43, 31, v42
	v_lshl_add_u64 v[60:61], v[2:3], 2, s[6:7]
	v_or_b32_e32 v2, 0x4c00, v9
	v_lshl_add_u64 v[58:59], v[42:43], 2, s[6:7]
	v_add_u32_e32 v42, v2, v8
	v_or_b32_e32 v2, v4, v2
	v_ashrrev_i32_e32 v43, 31, v42
	v_lshl_add_u64 v[64:65], v[2:3], 2, s[6:7]
	v_or_b32_e32 v2, 0x5000, v9
	v_lshl_add_u64 v[62:63], v[42:43], 2, s[6:7]
	global_load_dword v49, v[50:51], off
	global_load_dword v47, v[52:53], off
	global_load_dword v48, v[54:55], off
	global_load_dword v46, v[56:57], off
	global_load_dword v45, v[58:59], off
	global_load_dword v43, v[60:61], off
	global_load_dword v44, v[62:63], off
	global_load_dword v42, v[64:65], off
	v_add_u32_e32 v50, v2, v8
	v_or_b32_e32 v2, v4, v2
	v_ashrrev_i32_e32 v51, 31, v50
	v_lshl_add_u64 v[60:61], v[2:3], 2, s[6:7]
	v_or_b32_e32 v2, 0x5400, v9
	v_lshl_add_u64 v[58:59], v[50:51], 2, s[6:7]
	v_add_u32_e32 v50, v2, v8
	v_or_b32_e32 v2, v4, v2
	v_ashrrev_i32_e32 v51, 31, v50
	v_lshl_add_u64 v[64:65], v[2:3], 2, s[6:7]
	v_or_b32_e32 v2, 0x5800, v9
	v_lshl_add_u64 v[62:63], v[50:51], 2, s[6:7]
	v_add_u32_e32 v50, v2, v8
	v_or_b32_e32 v2, v4, v2
	v_ashrrev_i32_e32 v51, 31, v50
	v_lshl_add_u64 v[68:69], v[2:3], 2, s[6:7]
	v_or_b32_e32 v2, 0x5c00, v9
	v_lshl_add_u64 v[66:67], v[50:51], 2, s[6:7]
	v_add_u32_e32 v50, v2, v8
	v_or_b32_e32 v2, v4, v2
	v_ashrrev_i32_e32 v51, 31, v50
	v_lshl_add_u64 v[72:73], v[2:3], 2, s[6:7]
	v_or_b32_e32 v2, 0x6000, v9
	v_lshl_add_u64 v[70:71], v[50:51], 2, s[6:7]
	global_load_dword v57, v[58:59], off
	global_load_dword v55, v[60:61], off
	global_load_dword v56, v[62:63], off
	global_load_dword v54, v[64:65], off
	global_load_dword v53, v[66:67], off
	global_load_dword v51, v[68:69], off
	global_load_dword v52, v[70:71], off
	global_load_dword v50, v[72:73], off
	v_add_u32_e32 v58, v2, v8
	v_or_b32_e32 v2, v4, v2
	v_ashrrev_i32_e32 v59, 31, v58
	v_lshl_add_u64 v[68:69], v[2:3], 2, s[6:7]
	v_or_b32_e32 v2, 0x6400, v9
	v_lshl_add_u64 v[66:67], v[58:59], 2, s[6:7]
	v_add_u32_e32 v58, v2, v8
	v_or_b32_e32 v2, v4, v2
	v_ashrrev_i32_e32 v59, 31, v58
	v_lshl_add_u64 v[72:73], v[2:3], 2, s[6:7]
	v_or_b32_e32 v2, 0x6800, v9
	v_lshl_add_u64 v[70:71], v[58:59], 2, s[6:7]
	v_add_u32_e32 v58, v2, v8
	v_or_b32_e32 v2, v4, v2
	v_ashrrev_i32_e32 v59, 31, v58
	v_lshl_add_u64 v[76:77], v[2:3], 2, s[6:7]
	v_or_b32_e32 v2, 0x6c00, v9
	v_lshl_add_u64 v[74:75], v[58:59], 2, s[6:7]
	v_add_u32_e32 v58, v2, v8
	v_or_b32_e32 v2, v4, v2
	v_ashrrev_i32_e32 v59, 31, v58
	v_lshl_add_u64 v[80:81], v[2:3], 2, s[6:7]
	v_or_b32_e32 v2, 0x7000, v9
	v_lshl_add_u64 v[78:79], v[58:59], 2, s[6:7]
	global_load_dword v65, v[66:67], off
	global_load_dword v63, v[68:69], off
	global_load_dword v64, v[70:71], off
	global_load_dword v62, v[72:73], off
	global_load_dword v61, v[74:75], off
	global_load_dword v59, v[76:77], off
	global_load_dword v60, v[78:79], off
	global_load_dword v58, v[80:81], off
	v_add_u32_e32 v66, v2, v8
	v_or_b32_e32 v2, v4, v2
	v_ashrrev_i32_e32 v67, 31, v66
	v_lshl_add_u64 v[76:77], v[2:3], 2, s[6:7]
	v_or_b32_e32 v2, 0x7400, v9
	v_lshl_add_u64 v[74:75], v[66:67], 2, s[6:7]
	v_add_u32_e32 v66, v2, v8
	v_or_b32_e32 v2, v4, v2
	v_ashrrev_i32_e32 v67, 31, v66
	v_lshl_add_u64 v[80:81], v[2:3], 2, s[6:7]
	v_or_b32_e32 v2, 0x7800, v9
	v_lshl_add_u64 v[78:79], v[66:67], 2, s[6:7]
	v_add_u32_e32 v66, v2, v8
	v_or_b32_e32 v2, v4, v2
	v_ashrrev_i32_e32 v67, 31, v66
	v_lshl_add_u64 v[84:85], v[2:3], 2, s[6:7]
	v_or_b32_e32 v2, 0x7c00, v9
	v_lshl_add_u64 v[82:83], v[66:67], 2, s[6:7]
	v_add_u32_e32 v66, v2, v8
	v_or_b32_e32 v2, v4, v2
	v_ashrrev_i32_e32 v67, 31, v66
	v_lshl_add_u64 v[88:89], v[2:3], 2, s[6:7]
	v_or_b32_e32 v2, 0x8000, v9
	v_lshl_add_u64 v[86:87], v[66:67], 2, s[6:7]
	global_load_dword v73, v[74:75], off
	global_load_dword v71, v[76:77], off
	global_load_dword v72, v[78:79], off
	global_load_dword v70, v[80:81], off
	global_load_dword v69, v[82:83], off
	global_load_dword v67, v[84:85], off
	global_load_dword v68, v[86:87], off
	global_load_dword v66, v[88:89], off
	v_add_u32_e32 v74, v2, v8
	v_or_b32_e32 v2, v4, v2
	v_ashrrev_i32_e32 v75, 31, v74
	v_lshl_add_u64 v[84:85], v[2:3], 2, s[6:7]
	v_or_b32_e32 v2, 0x8400, v9
	v_lshl_add_u64 v[82:83], v[74:75], 2, s[6:7]
	v_add_u32_e32 v74, v2, v8
	v_or_b32_e32 v2, v4, v2
	v_ashrrev_i32_e32 v75, 31, v74
	v_lshl_add_u64 v[88:89], v[2:3], 2, s[6:7]
	v_or_b32_e32 v2, 0x8800, v9
	v_lshl_add_u64 v[86:87], v[74:75], 2, s[6:7]
	v_add_u32_e32 v74, v2, v8
	v_or_b32_e32 v2, v4, v2
	v_ashrrev_i32_e32 v75, 31, v74
	v_lshl_add_u64 v[92:93], v[2:3], 2, s[6:7]
	v_or_b32_e32 v2, 0x8c00, v9
	v_lshl_add_u64 v[90:91], v[74:75], 2, s[6:7]
	v_add_u32_e32 v74, v2, v8
	v_or_b32_e32 v2, v4, v2
	v_ashrrev_i32_e32 v75, 31, v74
	v_lshl_add_u64 v[96:97], v[2:3], 2, s[6:7]
	v_or_b32_e32 v2, 0x9000, v9
	v_lshl_add_u64 v[94:95], v[74:75], 2, s[6:7]
	global_load_dword v81, v[82:83], off
	global_load_dword v79, v[84:85], off
	global_load_dword v80, v[86:87], off
	global_load_dword v78, v[88:89], off
	global_load_dword v77, v[90:91], off
	global_load_dword v75, v[92:93], off
	global_load_dword v76, v[94:95], off
	global_load_dword v74, v[96:97], off
	v_add_u32_e32 v82, v2, v8
	v_or_b32_e32 v2, v4, v2
	v_ashrrev_i32_e32 v83, 31, v82
	v_lshl_add_u64 v[88:89], v[2:3], 2, s[6:7]
	v_or_b32_e32 v2, 0x9400, v9
	v_lshl_add_u64 v[86:87], v[82:83], 2, s[6:7]
	v_add_u32_e32 v82, v2, v8
	v_or_b32_e32 v2, v4, v2
	v_ashrrev_i32_e32 v83, 31, v82
	v_lshl_add_u64 v[92:93], v[2:3], 2, s[6:7]
	v_or_b32_e32 v2, 0x9800, v9
	v_lshl_add_u64 v[90:91], v[82:83], 2, s[6:7]
	v_add_u32_e32 v82, v2, v8
	v_or_b32_e32 v2, v4, v2
	v_ashrrev_i32_e32 v83, 31, v82
	v_lshl_add_u64 v[96:97], v[2:3], 2, s[6:7]
	v_or_b32_e32 v2, 0x9c00, v9
	v_lshl_add_u64 v[94:95], v[82:83], 2, s[6:7]
	v_add_u32_e32 v82, v2, v8
	v_or_b32_e32 v2, v4, v2
	v_ashrrev_i32_e32 v83, 31, v82
	v_lshl_add_u64 v[100:101], v[2:3], 2, s[6:7]
	v_or_b32_e32 v2, 0xa000, v9
	v_lshl_add_u64 v[98:99], v[82:83], 2, s[6:7]
	global_load_dword v85, v[86:87], off
	global_load_dword v102, v[88:89], off
	global_load_dword v103, v[90:91], off
	global_load_dword v104, v[92:93], off
	global_load_dword v105, v[94:95], off
	global_load_dword v83, v[96:97], off
	global_load_dword v84, v[98:99], off
	global_load_dword v82, v[100:101], off
	v_add_u32_e32 v86, v2, v8
	v_or_b32_e32 v2, v4, v2
	v_lshl_add_u64 v[88:89], v[2:3], 2, s[6:7]
	v_or_b32_e32 v2, 0xa400, v9
	v_add_u32_e32 v90, v2, v8
	v_or_b32_e32 v2, v4, v2
	v_lshl_add_u64 v[92:93], v[2:3], 2, s[6:7]
	v_or_b32_e32 v2, 0xa800, v9
	v_add_u32_e32 v94, v2, v8
	v_or_b32_e32 v2, v4, v2
	v_lshl_add_u64 v[96:97], v[2:3], 2, s[6:7]
	v_or_b32_e32 v2, 0xac00, v9
	v_ashrrev_i32_e32 v87, 31, v86
	v_add_u32_e32 v98, v2, v8
	v_or_b32_e32 v2, v4, v2
	v_lshl_add_u64 v[86:87], v[86:87], 2, s[6:7]
	v_ashrrev_i32_e32 v91, 31, v90
	v_ashrrev_i32_e32 v95, 31, v94
	v_ashrrev_i32_e32 v99, 31, v98
	v_lshl_add_u64 v[100:101], v[2:3], 2, s[6:7]
	v_or_b32_e32 v2, 0xb000, v9
	v_lshl_add_u64 v[90:91], v[90:91], 2, s[6:7]
	v_lshl_add_u64 v[94:95], v[94:95], 2, s[6:7]
	v_lshl_add_u64 v[98:99], v[98:99], 2, s[6:7]
	global_load_dword v106, v[86:87], off
	global_load_dword v107, v[88:89], off
	global_load_dword v108, v[90:91], off
	global_load_dword v109, v[92:93], off
	global_load_dword v110, v[94:95], off
	global_load_dword v111, v[96:97], off
	global_load_dword v112, v[98:99], off
	global_load_dword v113, v[100:101], off
	v_add_u32_e32 v86, v2, v8
	v_or_b32_e32 v2, v4, v2
	v_lshl_add_u64 v[88:89], v[2:3], 2, s[6:7]
	v_or_b32_e32 v2, 0xb400, v9
	v_add_u32_e32 v90, v2, v8
	v_or_b32_e32 v2, v4, v2
	v_lshl_add_u64 v[92:93], v[2:3], 2, s[6:7]
	v_or_b32_e32 v2, 0xb800, v9
	v_add_u32_e32 v94, v2, v8
	v_or_b32_e32 v2, v4, v2
	v_lshl_add_u64 v[96:97], v[2:3], 2, s[6:7]
	v_or_b32_e32 v2, 0xbc00, v9
	v_ashrrev_i32_e32 v87, 31, v86
	v_add_u32_e32 v98, v2, v8
	v_or_b32_e32 v2, v4, v2
	v_lshl_add_u64 v[86:87], v[86:87], 2, s[6:7]
	v_ashrrev_i32_e32 v91, 31, v90
	v_ashrrev_i32_e32 v95, 31, v94
	v_ashrrev_i32_e32 v99, 31, v98
	v_lshl_add_u64 v[100:101], v[2:3], 2, s[6:7]
	v_or_b32_e32 v2, 0xc000, v9
	v_lshl_add_u64 v[90:91], v[90:91], 2, s[6:7]
	v_lshl_add_u64 v[94:95], v[94:95], 2, s[6:7]
	v_lshl_add_u64 v[98:99], v[98:99], 2, s[6:7]
	global_load_dword v114, v[86:87], off
	global_load_dword v115, v[88:89], off
	global_load_dword v116, v[90:91], off
	global_load_dword v117, v[92:93], off
	global_load_dword v118, v[94:95], off
	global_load_dword v119, v[96:97], off
	global_load_dword v120, v[98:99], off
	global_load_dword v121, v[100:101], off
	v_add_u32_e32 v86, v2, v8
	v_or_b32_e32 v2, v4, v2
	v_lshl_add_u64 v[88:89], v[2:3], 2, s[6:7]
	v_or_b32_e32 v2, 0xc400, v9
	v_add_u32_e32 v90, v2, v8
	v_or_b32_e32 v2, v4, v2
	v_lshl_add_u64 v[92:93], v[2:3], 2, s[6:7]
	v_or_b32_e32 v2, 0xc800, v9
	v_add_u32_e32 v94, v2, v8
	v_or_b32_e32 v2, v4, v2
	v_lshl_add_u64 v[96:97], v[2:3], 2, s[6:7]
	v_or_b32_e32 v2, 0xcc00, v9
	v_ashrrev_i32_e32 v87, 31, v86
	v_add_u32_e32 v98, v2, v8
	v_or_b32_e32 v2, v4, v2
	v_lshl_add_u64 v[86:87], v[86:87], 2, s[6:7]
	v_ashrrev_i32_e32 v91, 31, v90
	v_ashrrev_i32_e32 v95, 31, v94
	v_ashrrev_i32_e32 v99, 31, v98
	v_lshl_add_u64 v[100:101], v[2:3], 2, s[6:7]
	v_or_b32_e32 v2, 0xd000, v9
	v_lshl_add_u64 v[90:91], v[90:91], 2, s[6:7]
	v_lshl_add_u64 v[94:95], v[94:95], 2, s[6:7]
	v_lshl_add_u64 v[98:99], v[98:99], 2, s[6:7]
	global_load_dword v122, v[86:87], off
	global_load_dword v123, v[88:89], off
	global_load_dword v124, v[90:91], off
	global_load_dword v125, v[92:93], off
	global_load_dword v126, v[94:95], off
	global_load_dword v127, v[96:97], off
	global_load_dword v128, v[98:99], off
	global_load_dword v129, v[100:101], off
	v_add_u32_e32 v86, v2, v8
	v_or_b32_e32 v2, v4, v2
	v_lshl_add_u64 v[88:89], v[2:3], 2, s[6:7]
	v_or_b32_e32 v2, 0xd400, v9
	v_add_u32_e32 v90, v2, v8
	v_or_b32_e32 v2, v4, v2
	v_lshl_add_u64 v[92:93], v[2:3], 2, s[6:7]
	v_or_b32_e32 v2, 0xd800, v9
	v_add_u32_e32 v94, v2, v8
	v_or_b32_e32 v2, v4, v2
	v_lshl_add_u64 v[96:97], v[2:3], 2, s[6:7]
	v_or_b32_e32 v2, 0xdc00, v9
	v_ashrrev_i32_e32 v87, 31, v86
	v_add_u32_e32 v98, v2, v8
	v_or_b32_e32 v2, v4, v2
	v_lshl_add_u64 v[86:87], v[86:87], 2, s[6:7]
	v_ashrrev_i32_e32 v91, 31, v90
	v_ashrrev_i32_e32 v95, 31, v94
	v_ashrrev_i32_e32 v99, 31, v98
	v_lshl_add_u64 v[100:101], v[2:3], 2, s[6:7]
	v_or_b32_e32 v2, 0xe000, v9
	v_lshl_add_u64 v[90:91], v[90:91], 2, s[6:7]
	v_lshl_add_u64 v[94:95], v[94:95], 2, s[6:7]
	v_lshl_add_u64 v[98:99], v[98:99], 2, s[6:7]
	global_load_dword v130, v[86:87], off
	global_load_dword v131, v[88:89], off
	global_load_dword v132, v[90:91], off
	global_load_dword v133, v[92:93], off
	global_load_dword v134, v[94:95], off
	global_load_dword v135, v[96:97], off
	global_load_dword v136, v[98:99], off
	global_load_dword v137, v[100:101], off
	v_add_u32_e32 v86, v2, v8
	v_or_b32_e32 v2, v4, v2
	v_lshl_add_u64 v[88:89], v[2:3], 2, s[6:7]
	v_or_b32_e32 v2, 0xe400, v9
	v_add_u32_e32 v90, v2, v8
	v_or_b32_e32 v2, v4, v2
	v_lshl_add_u64 v[92:93], v[2:3], 2, s[6:7]
	v_or_b32_e32 v2, 0xe800, v9
	v_add_u32_e32 v94, v2, v8
	v_or_b32_e32 v2, v4, v2
	v_lshl_add_u64 v[96:97], v[2:3], 2, s[6:7]
	v_or_b32_e32 v2, 0xec00, v9
	v_add_u32_e32 v98, v2, v8
	v_ashrrev_i32_e32 v87, 31, v86
	v_ashrrev_i32_e32 v99, 31, v98
	v_or_b32_e32 v2, v4, v2
	v_lshl_add_u64 v[86:87], v[86:87], 2, s[6:7]
	v_ashrrev_i32_e32 v91, 31, v90
	v_ashrrev_i32_e32 v95, 31, v94
	v_lshl_add_u64 v[98:99], v[98:99], 2, s[6:7]
	v_lshl_add_u64 v[100:101], v[2:3], 2, s[6:7]
	v_or_b32_e32 v2, 0xf000, v9
	v_lshl_add_u64 v[90:91], v[90:91], 2, s[6:7]
	v_lshl_add_u64 v[94:95], v[94:95], 2, s[6:7]
	global_load_dword v138, v[86:87], off
	global_load_dword v139, v[88:89], off
	global_load_dword v140, v[90:91], off
	global_load_dword v141, v[92:93], off
	global_load_dword v142, v[94:95], off
	global_load_dword v143, v[96:97], off
	s_nop 0
	global_load_dword v98, v[98:99], off
	s_nop 0
	global_load_dword v99, v[100:101], off
	v_add_u32_e32 v86, v2, v8
	v_or_b32_e32 v2, v4, v2
	v_lshl_add_u64 v[88:89], v[2:3], 2, s[6:7]
	v_or_b32_e32 v2, 0xf400, v9
	v_add_u32_e32 v90, v2, v8
	v_or_b32_e32 v2, v4, v2
	v_lshl_add_u64 v[92:93], v[2:3], 2, s[6:7]
	v_or_b32_e32 v2, 0xf800, v9
	v_add_u32_e32 v94, v2, v8
	v_or_b32_e32 v2, v4, v2
	v_lshl_add_u64 v[96:97], v[2:3], 2, s[6:7]
	v_or_b32_e32 v2, 0xfc00, v9
	v_add_u32_e32 v8, v2, v8
	v_ashrrev_i32_e32 v87, 31, v86
	v_ashrrev_i32_e32 v91, 31, v90
	v_ashrrev_i32_e32 v9, 31, v8
	v_lshl_add_u64 v[86:87], v[86:87], 2, s[6:7]
	v_lshl_add_u64 v[90:91], v[90:91], 2, s[6:7]
	v_ashrrev_i32_e32 v95, 31, v94
	v_lshl_add_u64 v[8:9], v[8:9], 2, s[6:7]
	v_or_b32_e32 v2, v4, v2
	v_lshl_add_u64 v[94:95], v[94:95], 2, s[6:7]
	v_lshl_add_u64 v[2:3], v[2:3], 2, s[6:7]
	global_load_dword v86, v[86:87], off
	s_nop 0
	global_load_dword v87, v[88:89], off
	s_nop 0
	global_load_dword v88, v[90:91], off
	global_load_dword v89, v[92:93], off
	s_nop 0
	global_load_dword v90, v[94:95], off
	global_load_dword v91, v[96:97], off
	s_nop 0
	global_load_dword v8, v[8:9], off
	s_nop 0
	global_load_dword v9, v[2:3], off
	s_andn2_b32 s3, s3, 31
	v_lshrrev_b32_e32 v92, 5, v0
	s_mov_b32 s12, 0x3fb8aa3b
	s_mov_b32 s10, 0xc2ce8ed0
	s_mov_b32 s11, 0x42b17218
	s_waitcnt vmcnt(63)
	v_mul_f32_e32 v146, 0x3fb8aa3b, v144
	v_mul_f32_e32 v147, 0x3fb8aa3b, v145
	v_fma_f32 v148, v144, s12, -v146
	v_rndne_f32_e32 v149, v146
	v_fma_f32 v150, v145, s12, -v147
	v_rndne_f32_e32 v151, v147
	v_fmac_f32_e32 v148, 0x32a5705f, v144
	v_sub_f32_e32 v146, v146, v149
	v_fmac_f32_e32 v150, 0x32a5705f, v145
	v_sub_f32_e32 v147, v147, v151
	v_add_f32_e32 v146, v146, v148
	v_cvt_i32_f32_e32 v149, v149
	v_add_f32_e32 v147, v147, v150
	v_exp_f32_e32 v146, v146
	v_cvt_i32_f32_e32 v151, v151
	v_exp_f32_e32 v147, v147
	v_cmp_ngt_f32_e32 vcc, s10, v144
	v_ldexp_f32 v146, v146, v149
	v_mov_b32_e32 v148, 0x7f800000
	v_ldexp_f32 v147, v147, v151
	v_cndmask_b32_e32 v146, 0, v146, vcc
	v_cmp_ngt_f32_e32 vcc, s10, v145
	s_nop 1
	v_cndmask_b32_e32 v147, 0, v147, vcc
	v_cmp_nlt_f32_e32 vcc, s11, v144
	s_nop 1
	v_cndmask_b32_e32 v144, v148, v146, vcc
	v_cmp_nlt_f32_e32 vcc, s11, v145
	s_nop 1
	v_cndmask_b32_e32 v145, v148, v147, vcc
	ds_write2st64_b32 v1, v144, v145 offset0:66 offset1:70
	s_waitcnt lgkmcnt(0)
	s_barrier
	v_lshlrev_b32_e32 v2, 2, v7
	v_lshl_or_b32 v2, v6, 9, v2
	v_add_u32_e32 v93, 0x4000, v2
	ds_read2_b32 v[2:3], v93 offset0:128 offset1:130
	s_movk_i32 s8, 0x84
	s_lshl_b32 s9, s2, 10
	s_mov_b64 s[6:7], 0
	s_waitcnt vmcnt(62) lgkmcnt(0)
	v_mul_f32_e32 v2, v15, v2
	s_nop 1
	v_mfma_f32_32x32x2_f32 a[0:15], v2, v16, 0
	v_mul_f32_e32 v2, v17, v3
	s_nop 1
	v_mfma_f32_32x32x2_f32 a[0:15], v2, v14, a[0:15]
	ds_read2_b32 v[2:3], v93 offset0:132 offset1:134
	s_waitcnt lgkmcnt(0)
	v_mul_f32_e32 v2, v13, v2
	s_nop 1
	v_mfma_f32_32x32x2_f32 a[0:15], v2, v11, a[0:15]
	v_mul_f32_e32 v2, v12, v3
	v_sub_u32_e32 v11, v4, v92
	s_nop 0
	v_mfma_f32_32x32x2_f32 a[0:15], v2, v10, a[0:15]
	ds_read2_b32 v[2:3], v93 offset0:136 offset1:138
	v_lshlrev_b32_e32 v10, 9, v92
	s_waitcnt lgkmcnt(0)
	v_mul_f32_e32 v2, v25, v2
	s_nop 1
	v_mfma_f32_32x32x2_f32 a[0:15], v2, v23, a[0:15]
	v_mul_f32_e32 v2, v24, v3
	s_nop 1
	v_mfma_f32_32x32x2_f32 a[0:15], v2, v22, a[0:15]
	ds_read2_b32 v[2:3], v93 offset0:140 offset1:142
	s_waitcnt lgkmcnt(0)
	v_mul_f32_e32 v2, v21, v2
	s_nop 1
	v_mfma_f32_32x32x2_f32 a[0:15], v2, v19, a[0:15]
	v_mul_f32_e32 v2, v20, v3
	s_nop 1
	v_mfma_f32_32x32x2_f32 a[0:15], v2, v18, a[0:15]
	ds_read2_b32 v[2:3], v93 offset0:144 offset1:146
	s_waitcnt lgkmcnt(0)
	v_mul_f32_e32 v2, v33, v2
	s_nop 1
	v_mfma_f32_32x32x2_f32 a[0:15], v2, v31, a[0:15]
	v_mul_f32_e32 v2, v32, v3
	s_nop 1
	v_mfma_f32_32x32x2_f32 a[0:15], v2, v30, a[0:15]
	ds_read2_b32 v[2:3], v93 offset0:148 offset1:150
	s_waitcnt lgkmcnt(0)
	v_mul_f32_e32 v2, v29, v2
	s_nop 1
	v_mfma_f32_32x32x2_f32 a[0:15], v2, v27, a[0:15]
	v_mul_f32_e32 v2, v28, v3
	s_nop 1
	v_mfma_f32_32x32x2_f32 a[0:15], v2, v26, a[0:15]
	ds_read2_b32 v[2:3], v93 offset0:152 offset1:154
	s_waitcnt lgkmcnt(0)
	v_mul_f32_e32 v2, v41, v2
	s_nop 1
	v_mfma_f32_32x32x2_f32 a[0:15], v2, v39, a[0:15]
	v_mul_f32_e32 v2, v40, v3
	s_nop 1
	v_mfma_f32_32x32x2_f32 a[0:15], v2, v38, a[0:15]
	ds_read2_b32 v[2:3], v93 offset0:156 offset1:158
	s_waitcnt lgkmcnt(0)
	v_mul_f32_e32 v2, v37, v2
	s_nop 1
	v_mfma_f32_32x32x2_f32 a[0:15], v2, v35, a[0:15]
	v_mul_f32_e32 v2, v36, v3
	s_nop 1
	v_mfma_f32_32x32x2_f32 a[0:15], v2, v34, a[0:15]
	ds_read2_b32 v[2:3], v93 offset0:160 offset1:162
	s_waitcnt lgkmcnt(0)
	v_mul_f32_e32 v2, v49, v2
	s_nop 1
	v_mfma_f32_32x32x2_f32 a[0:15], v2, v47, a[0:15]
	v_mul_f32_e32 v2, v48, v3
	s_nop 1
	v_mfma_f32_32x32x2_f32 a[0:15], v2, v46, a[0:15]
	ds_read2_b32 v[2:3], v93 offset0:164 offset1:166
	s_waitcnt lgkmcnt(0)
	v_mul_f32_e32 v2, v45, v2
	s_nop 1
	v_mfma_f32_32x32x2_f32 a[0:15], v2, v43, a[0:15]
	v_mul_f32_e32 v2, v44, v3
	s_nop 1
	v_mfma_f32_32x32x2_f32 a[0:15], v2, v42, a[0:15]
	ds_read2_b32 v[2:3], v93 offset0:168 offset1:170
	s_waitcnt lgkmcnt(0)
	v_mul_f32_e32 v2, v57, v2
	s_nop 1
	v_mfma_f32_32x32x2_f32 a[0:15], v2, v55, a[0:15]
	v_mul_f32_e32 v2, v56, v3
	s_nop 1
	v_mfma_f32_32x32x2_f32 a[0:15], v2, v54, a[0:15]
	ds_read2_b32 v[2:3], v93 offset0:172 offset1:174
	s_waitcnt lgkmcnt(0)
	v_mul_f32_e32 v2, v53, v2
	s_nop 1
	v_mfma_f32_32x32x2_f32 a[0:15], v2, v51, a[0:15]
	v_mul_f32_e32 v2, v52, v3
	s_nop 1
	v_mfma_f32_32x32x2_f32 a[0:15], v2, v50, a[0:15]
	ds_read2_b32 v[2:3], v93 offset0:176 offset1:178
	s_waitcnt lgkmcnt(0)
	v_mul_f32_e32 v2, v65, v2
	s_nop 1
	v_mfma_f32_32x32x2_f32 a[0:15], v2, v63, a[0:15]
	v_mul_f32_e32 v2, v64, v3
	s_nop 1
	v_mfma_f32_32x32x2_f32 a[0:15], v2, v62, a[0:15]
	ds_read2_b32 v[2:3], v93 offset0:180 offset1:182
	s_waitcnt lgkmcnt(0)
	v_mul_f32_e32 v2, v61, v2
	s_nop 1
	v_mfma_f32_32x32x2_f32 a[0:15], v2, v59, a[0:15]
	v_mul_f32_e32 v2, v60, v3
	s_nop 1
	v_mfma_f32_32x32x2_f32 a[0:15], v2, v58, a[0:15]
	ds_read2_b32 v[2:3], v93 offset0:184 offset1:186
	s_waitcnt lgkmcnt(0)
	v_mul_f32_e32 v2, v73, v2
	s_nop 1
	v_mfma_f32_32x32x2_f32 a[0:15], v2, v71, a[0:15]
	v_mul_f32_e32 v2, v72, v3
	s_nop 1
	v_mfma_f32_32x32x2_f32 a[0:15], v2, v70, a[0:15]
	ds_read2_b32 v[2:3], v93 offset0:188 offset1:190
	s_waitcnt lgkmcnt(0)
	v_mul_f32_e32 v2, v69, v2
	s_nop 1
	v_mfma_f32_32x32x2_f32 a[0:15], v2, v67, a[0:15]
	v_mul_f32_e32 v2, v68, v3
	s_nop 1
	v_mfma_f32_32x32x2_f32 a[0:15], v2, v66, a[0:15]
	ds_read2_b32 v[2:3], v93 offset0:192 offset1:194
	s_waitcnt lgkmcnt(0)
	v_mul_f32_e32 v2, v81, v2
	s_nop 1
	v_mfma_f32_32x32x2_f32 a[0:15], v2, v79, a[0:15]
	s_waitcnt vmcnt(61)
	v_mul_f32_e32 v2, v80, v3
	s_waitcnt vmcnt(60)
	s_nop 0
	v_mfma_f32_32x32x2_f32 a[0:15], v2, v78, a[0:15]
	ds_read2_b32 v[2:3], v93 offset0:196 offset1:198
	s_waitcnt vmcnt(59) lgkmcnt(0)
	v_mul_f32_e32 v2, v77, v2
	s_waitcnt vmcnt(58)
	s_nop 0
	v_mfma_f32_32x32x2_f32 a[0:15], v2, v75, a[0:15]
	s_waitcnt vmcnt(57)
	v_mul_f32_e32 v2, v76, v3
	s_waitcnt vmcnt(56)
	s_nop 0
	v_mfma_f32_32x32x2_f32 a[0:15], v2, v74, a[0:15]
	ds_read2_b32 v[2:3], v93 offset0:200 offset1:202
	s_waitcnt vmcnt(55) lgkmcnt(0)
	v_mul_f32_e32 v2, v85, v2
	s_waitcnt vmcnt(54)
	s_nop 0
	v_mfma_f32_32x32x2_f32 a[0:15], v2, v102, a[0:15]
	s_waitcnt vmcnt(53)
	v_mul_f32_e32 v2, v103, v3
	s_waitcnt vmcnt(52)
	s_nop 0
	v_mfma_f32_32x32x2_f32 a[0:15], v2, v104, a[0:15]
	ds_read2_b32 v[2:3], v93 offset0:204 offset1:206
	s_waitcnt vmcnt(51) lgkmcnt(0)
	v_mul_f32_e32 v2, v105, v2
	s_waitcnt vmcnt(50)
	s_nop 0
	v_mfma_f32_32x32x2_f32 a[0:15], v2, v83, a[0:15]
	s_waitcnt vmcnt(49)
	v_mul_f32_e32 v2, v84, v3
	s_waitcnt vmcnt(48)
	s_nop 0
	v_mfma_f32_32x32x2_f32 a[0:15], v2, v82, a[0:15]
	ds_read2_b32 v[2:3], v93 offset0:208 offset1:210
	s_waitcnt vmcnt(47) lgkmcnt(0)
	v_mul_f32_e32 v2, v106, v2
	s_waitcnt vmcnt(46)
	s_nop 0
	v_mfma_f32_32x32x2_f32 a[0:15], v2, v107, a[0:15]
	s_waitcnt vmcnt(45)
	v_mul_f32_e32 v2, v108, v3
	s_waitcnt vmcnt(44)
	s_nop 0
	v_mfma_f32_32x32x2_f32 a[0:15], v2, v109, a[0:15]
	ds_read2_b32 v[2:3], v93 offset0:212 offset1:214
	s_waitcnt vmcnt(43) lgkmcnt(0)
	v_mul_f32_e32 v2, v110, v2
	s_waitcnt vmcnt(42)
	s_nop 0
	v_mfma_f32_32x32x2_f32 a[0:15], v2, v111, a[0:15]
	s_waitcnt vmcnt(41)
	v_mul_f32_e32 v2, v112, v3
	s_waitcnt vmcnt(40)
	s_nop 0
	v_mfma_f32_32x32x2_f32 a[0:15], v2, v113, a[0:15]
	ds_read2_b32 v[2:3], v93 offset0:216 offset1:218
	s_waitcnt vmcnt(39) lgkmcnt(0)
	v_mul_f32_e32 v2, v114, v2
	s_waitcnt vmcnt(38)
	s_nop 0
	v_mfma_f32_32x32x2_f32 a[0:15], v2, v115, a[0:15]
	s_waitcnt vmcnt(37)
	v_mul_f32_e32 v2, v116, v3
	s_waitcnt vmcnt(36)
	s_nop 0
	v_mfma_f32_32x32x2_f32 a[0:15], v2, v117, a[0:15]
	ds_read2_b32 v[2:3], v93 offset0:220 offset1:222
	s_waitcnt vmcnt(35) lgkmcnt(0)
	v_mul_f32_e32 v2, v118, v2
	s_waitcnt vmcnt(34)
	s_nop 0
	v_mfma_f32_32x32x2_f32 a[0:15], v2, v119, a[0:15]
	s_waitcnt vmcnt(33)
	v_mul_f32_e32 v2, v120, v3
	s_waitcnt vmcnt(32)
	s_nop 0
	v_mfma_f32_32x32x2_f32 a[0:15], v2, v121, a[0:15]
	ds_read2_b32 v[2:3], v93 offset0:224 offset1:226
	s_waitcnt vmcnt(31) lgkmcnt(0)
	v_mul_f32_e32 v2, v122, v2
	s_waitcnt vmcnt(30)
	s_nop 0
	v_mfma_f32_32x32x2_f32 a[0:15], v2, v123, a[0:15]
	s_waitcnt vmcnt(29)
	v_mul_f32_e32 v2, v124, v3
	s_waitcnt vmcnt(28)
	s_nop 0
	v_mfma_f32_32x32x2_f32 a[0:15], v2, v125, a[0:15]
	ds_read2_b32 v[2:3], v93 offset0:228 offset1:230
	s_waitcnt vmcnt(27) lgkmcnt(0)
	v_mul_f32_e32 v2, v126, v2
	s_waitcnt vmcnt(26)
	s_nop 0
	v_mfma_f32_32x32x2_f32 a[0:15], v2, v127, a[0:15]
	s_waitcnt vmcnt(25)
	v_mul_f32_e32 v2, v128, v3
	s_waitcnt vmcnt(24)
	s_nop 0
	v_mfma_f32_32x32x2_f32 a[0:15], v2, v129, a[0:15]
	ds_read2_b32 v[2:3], v93 offset0:232 offset1:234
	s_waitcnt vmcnt(23) lgkmcnt(0)
	v_mul_f32_e32 v2, v130, v2
	s_waitcnt vmcnt(22)
	s_nop 0
	v_mfma_f32_32x32x2_f32 a[0:15], v2, v131, a[0:15]
	s_waitcnt vmcnt(21)
	v_mul_f32_e32 v2, v132, v3
	s_waitcnt vmcnt(20)
	s_nop 0
	v_mfma_f32_32x32x2_f32 a[0:15], v2, v133, a[0:15]
	ds_read2_b32 v[2:3], v93 offset0:236 offset1:238
	s_waitcnt vmcnt(19) lgkmcnt(0)
	v_mul_f32_e32 v2, v134, v2
	s_waitcnt vmcnt(18)
	s_nop 0
	v_mfma_f32_32x32x2_f32 a[0:15], v2, v135, a[0:15]
	s_waitcnt vmcnt(17)
	v_mul_f32_e32 v2, v136, v3
	s_waitcnt vmcnt(16)
	s_nop 0
	v_mfma_f32_32x32x2_f32 a[0:15], v2, v137, a[0:15]
	ds_read2_b32 v[2:3], v93 offset0:240 offset1:242
	s_waitcnt vmcnt(15) lgkmcnt(0)
	v_mul_f32_e32 v2, v138, v2
	s_waitcnt vmcnt(14)
	s_nop 0
	v_mfma_f32_32x32x2_f32 a[0:15], v2, v139, a[0:15]
	s_waitcnt vmcnt(13)
	v_mul_f32_e32 v2, v140, v3
	s_waitcnt vmcnt(12)
	s_nop 0
	v_mfma_f32_32x32x2_f32 a[0:15], v2, v141, a[0:15]
	ds_read2_b32 v[2:3], v93 offset0:244 offset1:246
	s_waitcnt vmcnt(11) lgkmcnt(0)
	v_mul_f32_e32 v2, v142, v2
	s_waitcnt vmcnt(10)
	s_nop 0
	v_mfma_f32_32x32x2_f32 a[0:15], v2, v143, a[0:15]
	s_waitcnt vmcnt(9)
	v_mul_f32_e32 v2, v98, v3
	s_waitcnt vmcnt(8)
	s_nop 0
	v_mfma_f32_32x32x2_f32 a[0:15], v2, v99, a[0:15]
	ds_read2_b32 v[2:3], v93 offset0:248 offset1:250
	s_waitcnt vmcnt(7) lgkmcnt(0)
	v_mul_f32_e32 v2, v86, v2
	s_waitcnt vmcnt(6)
	s_nop 0
	v_mfma_f32_32x32x2_f32 a[0:15], v2, v87, a[0:15]
	s_waitcnt vmcnt(5)
	v_mul_f32_e32 v2, v88, v3
	s_waitcnt vmcnt(4)
	s_nop 0
	v_mfma_f32_32x32x2_f32 a[0:15], v2, v89, a[0:15]
	ds_read2_b32 v[2:3], v93 offset0:252 offset1:254
	s_waitcnt vmcnt(3) lgkmcnt(0)
	v_mul_f32_e32 v2, v90, v2
	s_waitcnt vmcnt(1)
	v_mul_f32_e32 v3, v8, v3
	v_mfma_f32_32x32x2_f32 a[0:15], v2, v91, a[0:15]
	v_mul_u32_u24_e32 v2, 0x1080, v6
	v_mul_u32_u24_e32 v6, 0x210, v7
	v_lshlrev_b32_e32 v7, 2, v5
	v_add3_u32 v12, v2, v6, v7
	v_mad_u32_u24 v6, v92, s8, v7
	s_and_b32 s8, s9, 0xffffc000
	v_or_b32_e32 v5, 0xffffff00, v0
	v_subrev_u32_e32 v7, s3, v11
	v_or3_b32 v2, s8, v10, v4
	s_movk_i32 s3, 0x2ff
	s_waitcnt vmcnt(0)
	v_mfma_f32_32x32x2_f32 a[0:15], v3, v9, a[0:15]
	s_nop 15
	s_nop 1
	ds_write_b32 v12, a0
	ds_write_b32 v12, a1 offset:132
	ds_write_b32 v12, a2 offset:264
	ds_write_b32 v12, a3 offset:396
	ds_write_b32 v12, a4 offset:1056
	ds_write_b32 v12, a5 offset:1188
	ds_write_b32 v12, a6 offset:1320
	ds_write_b32 v12, a7 offset:1452
	ds_write_b32 v12, a8 offset:2112
	ds_write_b32 v12, a9 offset:2244
	ds_write_b32 v12, a10 offset:2376
	ds_write_b32 v12, a11 offset:2508
	ds_write_b32 v12, a12 offset:3168
	ds_write_b32 v12, a13 offset:3300
	ds_write_b32 v12, a14 offset:3432
	ds_write_b32 v12, a15 offset:3564
	s_waitcnt lgkmcnt(0)
	s_barrier

	.amdhsa_kernel _Z9k_gemm_byPKfS0_S0_PfS1_Pd
		.amdhsa_group_segment_fixed_size 18944
		.amdhsa_private_segment_fixed_size 0
		.amdhsa_kernarg_size 48
		.amdhsa_user_sgpr_count 2
		.amdhsa_user_sgpr_dispatch_ptr 0
		.amdhsa_user_sgpr_queue_ptr 0
		.amdhsa_user_sgpr_kernarg_segment_ptr 1
		.amdhsa_user_sgpr_dispatch_id 0
		.amdhsa_user_sgpr_kernarg_preload_length 0
		.amdhsa_user_sgpr_kernarg_preload_offset 0
		.amdhsa_user_sgpr_private_segment_size 0
		.amdhsa_uses_dynamic_stack 0
		.amdhsa_enable_private_segment 0
		.amdhsa_system_sgpr_workgroup_id_x 1
		.amdhsa_system_sgpr_workgroup_id_y 0
		.amdhsa_system_sgpr_workgroup_id_z 0
		.amdhsa_system_sgpr_workgroup_info 0
		.amdhsa_system_vgpr_workitem_id 0
		.amdhsa_next_free_vgpr 168
		.amdhsa_next_free_sgpr 16
		.amdhsa_accum_offset 152
		.amdhsa_reserve_vcc 1
		.amdhsa_float_round_mode_32 0
		.amdhsa_float_round_mode_16_64 0
		.amdhsa_float_denorm_mode_32 3
		.amdhsa_float_denorm_mode_16_64 3
		.amdhsa_dx10_clamp 1
		.amdhsa_ieee_mode 1
		.amdhsa_fp16_overflow 0
		.amdhsa_tg_split 0
		.amdhsa_exception_fp_ieee_invalid_op 0
		.amdhsa_exception_fp_denorm_src 0
		.amdhsa_exception_fp_ieee_div_zero 0
		.amdhsa_exception_fp_ieee_overflow 0
		.amdhsa_exception_fp_ieee_underflow 0
		.amdhsa_exception_fp_ieee_inexact 0
		.amdhsa_exception_int_div_zero 0
	.end_amdhsa_kernel

amdhsa.kernels:
  - .agpr_count:     16
    .args:
      - .actual_access:  read_only
        .address_space:  global
        .offset:         0
        .size:           8
        .value_kind:     global_buffer
      - .actual_access:  read_only
        .address_space:  global
        .offset:         8
        .size:           8
        .value_kind:     global_buffer
      - .actual_access:  read_only
        .address_space:  global
        .offset:         16
        .size:           8
        .value_kind:     global_buffer
      - .actual_access:  write_only
        .address_space:  global
        .offset:         24
        .size:           8
        .value_kind:     global_buffer
      - .actual_access:  write_only
        .address_space:  global
        .offset:         32
        .size:           8
        .value_kind:     global_buffer
      - .actual_access:  write_only
        .address_space:  global
        .offset:         40
        .size:           8
        .value_kind:     global_buffer
    .group_segment_fixed_size: 18944
    .kernarg_segment_align: 8
    .kernarg_segment_size: 48
    .language:       OpenCL C
    .language_version:
      - 2
      - 0
    .max_flat_workgroup_size: 256
    .name:           _Z9k_gemm_byPKfS0_S0_PfS1_Pd
    .private_segment_fixed_size: 0
    .sgpr_count:     22
    .sgpr_spill_count: 0
    .symbol:         _Z9k_gemm_byPKfS0_S0_PfS1_Pd.kd
    .uniform_work_group_size: 1
    .uses_dynamic_stack: false
    .vgpr_count:     168
    .vgpr_spill_count: 0
    .wavefront_size: 64
  - .agpr_count:     48
    .args:
      - .address_space:  global
        .offset:         0
        .size:           8
        .value_kind:     global_buffer
      - .address_space:  global
        .offset:         8
        .size:           8
        .value_kind:     global_buffer
      - .address_space:  global
        .offset:         16
        .size:           8
        .value_kind:     global_buffer
      - .address_space:  global
        .offset:         24
        .size:           8
        .value_kind:     global_buffer
      - .actual_access:  write_only
        .address_space:  global
        .offset:         32
        .size:           8
        .value_kind:     global_buffer
      - .offset:         40
        .size:           4
        .value_kind:     by_value
      - .actual_access:  read_only
        .address_space:  global
        .offset:         48
        .size:           8
        .value_kind:     global_buffer
      - .actual_access:  read_only
        .address_space:  global
        .offset:         56
        .size:           8
        .value_kind:     global_buffer
      - .actual_access:  read_only
        .address_space:  global
        .offset:         64
        .size:           8
        .value_kind:     global_buffer
      - .address_space:  global
        .offset:         72
        .size:           8
        .value_kind:     global_buffer
      - .offset:         80
        .size:           4
        .value_kind:     by_value
      - .actual_access:  write_only
        .address_space:  global
        .offset:         88
        .size:           8
        .value_kind:     global_buffer
      - .actual_access:  write_only
        .address_space:  global
        .offset:         96
        .size:           8
        .value_kind:     global_buffer
      - .actual_access:  write_only
        .address_space:  global
        .offset:         104
        .size:           8
        .value_kind:     global_buffer
    .group_segment_fixed_size: 139520
    .kernarg_segment_align: 8
    .kernarg_segment_size: 112
    .language:       OpenCL C
    .language_version:
      - 2
      - 0
    .max_flat_workgroup_size: 256
    .name:           _Z7k_chol2PfS_S_S_PdiPKfS2_S2_S_iS_PDF16_S_
    .private_segment_fixed_size: 0
    .sgpr_count:     106
    .sgpr_spill_count: 0
    .symbol:         _Z7k_chol2PfS_S_S_PdiPKfS2_S2_S_iS_PDF16_S_.kd
    .uniform_work_group_size: 1
    .uses_dynamic_stack: false
    .vgpr_count:     252
    .vgpr_spill_count: 0
    .wavefront_size: 64
  - .agpr_count:     16
    .args:
      - .actual_access:  read_only
        .address_space:  global
        .offset:         0
        .size:           8
        .value_kind:     global_buffer
      - .address_space:  global
        .offset:         8
        .size:           8
        .value_kind:     global_buffer
      - .address_space:  global
        .offset:         16
        .size:           8
        .value_kind:     global_buffer
      - .actual_access:  read_only
        .address_space:  global
        .offset:         24
        .size:           8
        .value_kind:     global_buffer
      - .actual_access:  write_only
        .address_space:  global
        .offset:         32
        .size:           8
        .value_kind:     global_buffer
      - .actual_access:  write_only
        .address_space:  global
        .offset:         40
        .size:           8
        .value_kind:     global_buffer
      - .actual_access:  write_only
        .address_space:  global
        .offset:         48
        .size:           8
        .value_kind:     global_buffer
    .group_segment_fixed_size: 79872
    .kernarg_segment_align: 8
    .kernarg_segment_size: 56
    .language:       OpenCL C
    .language_version:
      - 2
      - 0
    .max_flat_workgroup_size: 256
    .name:           _Z6k_tailPKfPfS1_S0_S1_PDF16_S1_
    .private_segment_fixed_size: 0
    .sgpr_count:     34
    .sgpr_spill_count: 0
    .symbol:         _Z6k_tailPKfPfS1_S0_S1_PDF16_S1_.kd
    .uniform_work_group_size: 1
    .uses_dynamic_stack: false
    .vgpr_count:     152
    .vgpr_spill_count: 0
    .wavefront_size: 64
  - .agpr_count:     0
    .args:
      - .actual_access:  read_only
        .address_space:  global
        .offset:         0
        .size:           8
        .value_kind:     global_buffer
      - .actual_access:  read_only
        .address_space:  global
        .offset:         8
        .size:           8
        .value_kind:     global_buffer
      - .actual_access:  read_only
        .address_space:  global
        .offset:         16
        .size:           8
        .value_kind:     global_buffer
      - .actual_access:  write_only
        .address_space:  global
        .offset:         24
        .size:           8
        .value_kind:     global_buffer
      - .actual_access:  write_only
        .address_space:  global
        .offset:         32
        .size:           8
        .value_kind:     global_buffer
      - .actual_access:  write_only
        .address_space:  global
        .offset:         40
        .size:           8
        .value_kind:     global_buffer
    .group_segment_fixed_size: 16896
    .kernarg_segment_align: 8
    .kernarg_segment_size: 48
    .language:       OpenCL C
    .language_version:
      - 2
      - 0
    .max_flat_workgroup_size: 256
    .name:           _Z6k_prepPKfS0_S0_PfPDF16_S1_
    .private_segment_fixed_size: 0
    .sgpr_count:     28
    .sgpr_spill_count: 0
    .symbol:         _Z6k_prepPKfS0_S0_PfPDF16_S1_.kd
    .uniform_work_group_size: 1
    .uses_dynamic_stack: false
    .vgpr_count:     150
    .vgpr_spill_count: 0
    .wavefront_size: 64
  - .agpr_count:     0
    .args:
      - .actual_access:  read_only
        .address_space:  global
        .offset:         0
        .size:           8
        .value_kind:     global_buffer
      - .actual_access:  read_only
        .address_space:  global
        .offset:         8
        .size:           8
        .value_kind:     global_buffer
      - .actual_access:  read_only
        .address_space:  global
        .offset:         16
        .size:           8
        .value_kind:     global_buffer
      - .actual_access:  read_only
        .address_space:  global
        .offset:         24
        .size:           8
        .value_kind:     global_buffer
      - .actual_access:  write_only
        .address_space:  global
        .offset:         32
        .size:           8
        .value_kind:     global_buffer
      - .actual_access:  write_only
        .address_space:  global
        .offset:         40
        .size:           8
        .value_kind:     global_buffer
    .group_segment_fixed_size: 111616
    .kernarg_segment_align: 8
    .kernarg_segment_size: 48
    .language:       OpenCL C
    .language_version:
      - 2
      - 0
    .max_flat_workgroup_size: 512
    .name:           _Z6k_mainPKfS0_PKDF16_S0_PfPd
    .private_segment_fixed_size: 0
    .sgpr_count:     25
    .sgpr_spill_count: 0
    .symbol:         _Z6k_mainPKfS0_PKDF16_S0_PfPd.kd
    .uniform_work_group_size: 1
    .uses_dynamic_stack: false
    .vgpr_count:     246
    .vgpr_spill_count: 0
    .wavefront_size: 64
  - .agpr_count:     0
    .args:
      - .actual_access:  read_only
        .address_space:  global
        .offset:         0
        .size:           8
        .value_kind:     global_buffer
      - .actual_access:  write_only
        .address_space:  global
        .offset:         8
        .size:           8
        .value_kind:     global_buffer
    .group_segment_fixed_size: 0
    .kernarg_segment_align: 8
    .kernarg_segment_size: 16
    .language:       OpenCL C
    .language_version:
      - 2
      - 0
    .max_flat_workgroup_size: 1024
    .name:           _Z7k_finalPKdPf
    .private_segment_fixed_size: 0
    .sgpr_count:     28
    .sgpr_spill_count: 0
    .symbol:         _Z7k_finalPKdPf.kd
    .uniform_work_group_size: 1
    .uses_dynamic_stack: false
    .vgpr_count:     60
    .vgpr_spill_count: 0
    .wavefront_size: 64
